# v42 + screening MFMA as two interleaved accumulation chains
# speedup vs baseline: 1.0254x; 1.0047x over previous
.LBB0_118:
	s_waitcnt vmcnt(0)
	v_lshrrev_b32_e32 v67, 4, v0
	v_mov_b32_e32 v66, 0x11100
	v_lshl_or_b32 v66, v67, 2, v66
	s_waitcnt lgkmcnt(0)
	s_barrier
	ds_read_b32 v66, v66
	v_mul_u32_u24_e32 v68, 0x102, v67
	v_lshlrev_b32_e32 v72, 3, v68
	s_waitcnt lgkmcnt(0)
	v_max_i32_e32 v66, 1, v66
	v_cvt_f32_u32_e32 v66, v66
	v_div_scale_f32 v69, s[0:1], v66, v66, 1.0
	v_rcp_f32_e32 v70, v69
	v_div_scale_f32 v68, vcc, 1.0, v66, 1.0
	v_fma_f32 v71, -v69, v70, 1.0
	v_fmac_f32_e32 v70, v71, v70
	v_mul_f32_e32 v71, v68, v70
	v_fma_f32 v73, -v69, v71, v68
	v_fmac_f32_e32 v71, v73, v70
	v_fma_f32 v68, -v69, v71, v68
	v_div_fmas_f32 v73, v68, v70, v71
	v_lshl_add_u32 v68, v138, 3, v72
	v_add_u32_e32 v76, 0x8000, v68
	ds_read2_b64 v[68:71], v76 offset1:16
	v_div_fixup_f32 v77, v73, v66, 1.0
	v_mul_i32_i24_e32 v73, 0xfffffbf8, v67
	v_lshlrev_b32_e32 v66, 2, v138
	v_add3_u32 v78, v72, v73, v66
	ds_read2_b64 v[72:75], v76 offset0:32 offset1:48
	s_waitcnt lgkmcnt(1)
	v_cvt_f32_f64_e32 v68, v[68:69]
	v_cvt_f32_f64_e32 v69, v[70:71]
	v_mul_f32_e32 v68, v77, v68
	v_mul_f32_e32 v69, v77, v69
	v_fma_f32 v79, v68, v68, 0
	ds_write2_b32 v78, v68, v69 offset1:16
	s_waitcnt lgkmcnt(1)
	v_cvt_f32_f64_e32 v68, v[72:73]
	v_fmac_f32_e32 v79, v69, v69
	v_mul_f32_e32 v72, v77, v68
	ds_read2_b64 v[68:71], v76 offset0:64 offset1:80
	v_cvt_f32_f64_e32 v73, v[74:75]
	v_fmac_f32_e32 v79, v72, v72
	v_mul_f32_e32 v73, v77, v73
	v_fmac_f32_e32 v79, v73, v73
	ds_write2_b32 v78, v72, v73 offset0:32 offset1:48
	ds_read2_b64 v[72:75], v76 offset0:96 offset1:112
	s_waitcnt lgkmcnt(2)
	v_cvt_f32_f64_e32 v68, v[68:69]
	v_cvt_f32_f64_e32 v69, v[70:71]
	v_mul_f32_e32 v68, v77, v68
	v_mul_f32_e32 v69, v77, v69
	v_fmac_f32_e32 v79, v68, v68
	ds_write2_b32 v78, v68, v69 offset0:64 offset1:80
	s_waitcnt lgkmcnt(1)
	v_cvt_f32_f64_e32 v68, v[72:73]
	v_fmac_f32_e32 v79, v69, v69
	v_mul_f32_e32 v72, v77, v68
	ds_read2_b64 v[68:71], v76 offset0:128 offset1:144
	v_cvt_f32_f64_e32 v73, v[74:75]
	v_fmac_f32_e32 v79, v72, v72
	v_mul_f32_e32 v73, v77, v73
	v_fmac_f32_e32 v79, v73, v73
	ds_write2_b32 v78, v72, v73 offset0:96 offset1:112
	ds_read2_b64 v[72:75], v76 offset0:160 offset1:176
	s_waitcnt lgkmcnt(2)
	v_cvt_f32_f64_e32 v68, v[68:69]
	v_cvt_f32_f64_e32 v69, v[70:71]
	v_mul_f32_e32 v68, v77, v68
	v_mul_f32_e32 v69, v77, v69
	v_fmac_f32_e32 v79, v68, v68
	ds_write2_b32 v78, v68, v69 offset0:128 offset1:144
	s_waitcnt lgkmcnt(1)
	v_cvt_f32_f64_e32 v68, v[72:73]
	v_fmac_f32_e32 v79, v69, v69
	v_mul_f32_e32 v72, v77, v68
	ds_read2_b64 v[68:71], v76 offset0:192 offset1:208
	v_cvt_f32_f64_e32 v73, v[74:75]
	v_fmac_f32_e32 v79, v72, v72
	v_mul_f32_e32 v73, v77, v73
	v_fmac_f32_e32 v79, v73, v73
	ds_write2_b32 v78, v72, v73 offset0:160 offset1:176
	ds_read2_b64 v[72:75], v76 offset0:224 offset1:240
	s_waitcnt lgkmcnt(2)
	v_cvt_f32_f64_e32 v68, v[68:69]
	v_cvt_f32_f64_e32 v69, v[70:71]
	v_mul_f32_e32 v68, v77, v68
	v_mul_f32_e32 v69, v77, v69
	v_fmac_f32_e32 v79, v68, v68
	ds_write2_b32 v78, v68, v69 offset0:192 offset1:208
	s_waitcnt lgkmcnt(1)
	v_cvt_f32_f64_e32 v68, v[72:73]
	v_fmac_f32_e32 v79, v69, v69
	v_mul_f32_e32 v68, v77, v68
	v_cvt_f32_f64_e32 v69, v[74:75]
	v_fmac_f32_e32 v79, v68, v68
	v_mul_f32_e32 v69, v77, v69
	v_fmac_f32_e32 v79, v69, v69
	ds_write2_b32 v78, v68, v69 offset0:224 offset1:240
	v_cmp_eq_u32_e32 vcc, 0, v138
	v_add_f32_dpp v68, v79, v79 quad_perm:[1,0,3,2] row_mask:0xf bank_mask:0xf bound_ctrl:1
	s_nop 1
	v_add_f32_dpp v68, v68, v68 quad_perm:[2,3,0,1] row_mask:0xf bank_mask:0xf bound_ctrl:1
	s_nop 1
	v_add_f32_dpp v68, v68, v68 row_half_mirror row_mask:0xf bank_mask:0xf bound_ctrl:1
	s_nop 1
	v_mov_b32_dpp v69, v68 row_mirror row_mask:0xf bank_mask:0xf bound_ctrl:1
	s_and_saveexec_b64 s[0:1], vcc
	v_mov_b32_e32 v70, 0x11200
	v_lshl_or_b32 v67, v67, 2, v70
	v_add_f32_e32 v68, v68, v69
	ds_write_b32 v67, v68
	s_or_b64 exec, exec, s[0:1]
	v_lshlrev_b32_e32 v67, 2, v140
	s_movk_i32 s0, 0x408
	v_mad_u32_u24 v67, v138, s0, v67
	s_waitcnt lgkmcnt(0)
	s_barrier
	ds_read2_b32 v[68:69], v67 offset1:4
	ds_read2_b32 v[70:71], v67 offset0:64 offset1:68
	ds_read2_b32 v[72:73], v67 offset0:192 offset1:196
	s_lshl_b32 s29, s17, 2
	s_lshl_b32 s0, s24, 2
	s_waitcnt lgkmcnt(2)
	v_mfma_f32_16x16x4_f32 a[0:3], v68, v62, 0
	s_add_i32 s0, s0, 0x10100
	s_waitcnt lgkmcnt(1)
	v_mfma_f32_16x16x4_f32 a[4:7], v70, v63, 0
	ds_read2_b32 v[62:63], v67 offset0:128 offset1:132
	s_waitcnt lgkmcnt(0)
	v_mfma_f32_16x16x4_f32 a[0:3], v62, v64, a[0:3]
	v_mfma_f32_16x16x4_f32 a[4:7], v72, v65, a[4:7]
	v_mfma_f32_16x16x4_f32 a[0:3], v69, v58, a[0:3]
	v_mfma_f32_16x16x4_f32 a[4:7], v71, v59, a[4:7]
	ds_read2_b32 v[58:59], v67 offset0:8 offset1:12
	v_mfma_f32_16x16x4_f32 a[0:3], v63, v60, a[0:3]
	ds_read2_b32 v[62:63], v67 offset0:200 offset1:204
	v_mfma_f32_16x16x4_f32 a[4:7], v73, v61, a[4:7]
	ds_read2_b32 v[60:61], v67 offset0:72 offset1:76
	s_waitcnt lgkmcnt(2)
	v_mfma_f32_16x16x4_f32 a[0:3], v58, v54, a[0:3]
	s_waitcnt lgkmcnt(0)
	v_mfma_f32_16x16x4_f32 a[4:7], v60, v55, a[4:7]
	ds_read2_b32 v[54:55], v67 offset0:136 offset1:140
	s_waitcnt lgkmcnt(0)
	v_mfma_f32_16x16x4_f32 a[0:3], v54, v56, a[0:3]
	v_mfma_f32_16x16x4_f32 a[4:7], v62, v57, a[4:7]
	v_mfma_f32_16x16x4_f32 a[0:3], v59, v50, a[0:3]
	v_mfma_f32_16x16x4_f32 a[4:7], v61, v51, a[4:7]
	ds_read2_b32 v[50:51], v67 offset0:16 offset1:20
	v_mfma_f32_16x16x4_f32 a[0:3], v55, v52, a[0:3]
	ds_read2_b32 v[54:55], v67 offset0:208 offset1:212
	v_mfma_f32_16x16x4_f32 a[4:7], v63, v53, a[4:7]
	ds_read2_b32 v[52:53], v67 offset0:80 offset1:84
	s_waitcnt lgkmcnt(2)
	v_mfma_f32_16x16x4_f32 a[0:3], v50, v46, a[0:3]
	s_waitcnt lgkmcnt(0)
	v_mfma_f32_16x16x4_f32 a[4:7], v52, v47, a[4:7]
	ds_read2_b32 v[46:47], v67 offset0:144 offset1:148
	s_waitcnt lgkmcnt(0)
	v_mfma_f32_16x16x4_f32 a[0:3], v46, v48, a[0:3]
	v_mfma_f32_16x16x4_f32 a[4:7], v54, v49, a[4:7]
	v_mfma_f32_16x16x4_f32 a[0:3], v51, v42, a[0:3]
	v_mfma_f32_16x16x4_f32 a[4:7], v53, v43, a[4:7]
	ds_read2_b32 v[42:43], v67 offset0:24 offset1:28
	v_mfma_f32_16x16x4_f32 a[0:3], v47, v44, a[0:3]
	ds_read2_b32 v[46:47], v67 offset0:216 offset1:220
	v_mfma_f32_16x16x4_f32 a[4:7], v55, v45, a[4:7]
	ds_read2_b32 v[44:45], v67 offset0:88 offset1:92
	s_waitcnt lgkmcnt(2)
	v_mfma_f32_16x16x4_f32 a[0:3], v42, v38, a[0:3]
	s_waitcnt lgkmcnt(0)
	v_mfma_f32_16x16x4_f32 a[4:7], v44, v39, a[4:7]
	ds_read2_b32 v[38:39], v67 offset0:152 offset1:156
	s_waitcnt lgkmcnt(0)
	v_mfma_f32_16x16x4_f32 a[0:3], v38, v40, a[0:3]
	v_mfma_f32_16x16x4_f32 a[4:7], v46, v41, a[4:7]
	v_mfma_f32_16x16x4_f32 a[0:3], v43, v34, a[0:3]
	v_mfma_f32_16x16x4_f32 a[4:7], v45, v35, a[4:7]
	ds_read2_b32 v[34:35], v67 offset0:32 offset1:36
	v_mfma_f32_16x16x4_f32 a[0:3], v39, v36, a[0:3]
	ds_read2_b32 v[38:39], v67 offset0:224 offset1:228
	v_mfma_f32_16x16x4_f32 a[4:7], v47, v37, a[4:7]
	ds_read2_b32 v[36:37], v67 offset0:96 offset1:100
	s_waitcnt lgkmcnt(2)
	v_mfma_f32_16x16x4_f32 a[0:3], v34, v30, a[0:3]
	s_waitcnt lgkmcnt(0)
	v_mfma_f32_16x16x4_f32 a[4:7], v36, v31, a[4:7]
	ds_read2_b32 v[30:31], v67 offset0:160 offset1:164
	s_waitcnt lgkmcnt(0)
	v_mfma_f32_16x16x4_f32 a[0:3], v30, v32, a[0:3]
	v_mfma_f32_16x16x4_f32 a[4:7], v38, v33, a[4:7]
	v_mfma_f32_16x16x4_f32 a[0:3], v35, v26, a[0:3]
	v_mfma_f32_16x16x4_f32 a[4:7], v37, v27, a[4:7]
	ds_read2_b32 v[26:27], v67 offset0:40 offset1:44
	v_mfma_f32_16x16x4_f32 a[0:3], v31, v28, a[0:3]
	ds_read2_b32 v[30:31], v67 offset0:232 offset1:236
	v_mfma_f32_16x16x4_f32 a[4:7], v39, v29, a[4:7]
	ds_read2_b32 v[28:29], v67 offset0:104 offset1:108
	s_waitcnt lgkmcnt(2)
	v_mfma_f32_16x16x4_f32 a[0:3], v26, v22, a[0:3]
	s_waitcnt lgkmcnt(0)
	v_mfma_f32_16x16x4_f32 a[4:7], v28, v23, a[4:7]
	ds_read2_b32 v[22:23], v67 offset0:168 offset1:172
	s_waitcnt lgkmcnt(0)
	v_mfma_f32_16x16x4_f32 a[0:3], v22, v24, a[0:3]
	v_mfma_f32_16x16x4_f32 a[4:7], v30, v25, a[4:7]
	v_mfma_f32_16x16x4_f32 a[0:3], v27, v18, a[0:3]
	v_mfma_f32_16x16x4_f32 a[4:7], v29, v19, a[4:7]
	ds_read2_b32 v[18:19], v67 offset0:48 offset1:52
	v_mfma_f32_16x16x4_f32 a[0:3], v23, v20, a[0:3]
	ds_read2_b32 v[22:23], v67 offset0:240 offset1:244
	v_mfma_f32_16x16x4_f32 a[4:7], v31, v21, a[4:7]
	ds_read2_b32 v[20:21], v67 offset0:112 offset1:116
	s_waitcnt lgkmcnt(2)
	v_mfma_f32_16x16x4_f32 a[0:3], v18, v14, a[0:3]
	s_waitcnt lgkmcnt(0)
	v_mfma_f32_16x16x4_f32 a[4:7], v20, v15, a[4:7]
	ds_read2_b32 v[14:15], v67 offset0:176 offset1:180
	s_waitcnt lgkmcnt(0)
	v_mfma_f32_16x16x4_f32 a[0:3], v14, v16, a[0:3]
	v_mfma_f32_16x16x4_f32 a[4:7], v22, v17, a[4:7]
	v_mfma_f32_16x16x4_f32 a[0:3], v19, v10, a[0:3]
	v_mfma_f32_16x16x4_f32 a[4:7], v21, v11, a[4:7]
	ds_read2_b32 v[10:11], v67 offset0:56 offset1:60
	v_mfma_f32_16x16x4_f32 a[0:3], v15, v12, a[0:3]
	ds_read2_b32 v[14:15], v67 offset0:248 offset1:252
	v_mfma_f32_16x16x4_f32 a[4:7], v23, v13, a[4:7]
	ds_read2_b32 v[12:13], v67 offset0:120 offset1:124
	s_waitcnt lgkmcnt(2)
	v_mfma_f32_16x16x4_f32 a[0:3], v10, v6, a[0:3]
	s_waitcnt lgkmcnt(0)
	v_mfma_f32_16x16x4_f32 a[4:7], v12, v7, a[4:7]
	ds_read2_b32 v[6:7], v67 offset0:184 offset1:188
	s_waitcnt lgkmcnt(0)
	v_mfma_f32_16x16x4_f32 a[0:3], v6, v8, a[0:3]
	v_mfma_f32_16x16x4_f32 a[4:7], v14, v9, a[4:7]
	v_mfma_f32_16x16x4_f32 a[0:3], v11, v2, a[0:3]
	v_mov_b32_e32 v2, 0x11300
	v_lshl_add_u32 v2, v134, 2, v2
	ds_read_b32 v2, v2
	v_mfma_f32_16x16x4_f32 a[4:7], v13, v3, a[4:7]
	v_lshlrev_b32_e32 v3, 10, v140
	v_add3_u32 v3, s0, v66, v3
	v_mfma_f32_16x16x4_f32 a[0:3], v7, v4, a[0:3]
	v_or_b32_e32 v7, s29, v140
	v_lshl_or_b32 v4, v7, 8, v66
	v_add_u32_e32 v4, 0x10100, v4
	v_mfma_f32_16x16x4_f32 a[4:7], v15, v5, a[4:7]
	s_nop 9
	v_accvgpr_read_b32 v5, a0
	v_accvgpr_read_b32 v6, a1
	v_accvgpr_read_b32 v8, a2
	v_accvgpr_read_b32 v9, a3
	v_accvgpr_read_b32 v70, a4
	v_accvgpr_read_b32 v71, a5
	v_accvgpr_read_b32 v72, a6
	v_accvgpr_read_b32 v73, a7
	v_add_f32_e32 v5, v5, v70
	v_add_f32_e32 v6, v6, v71
	v_add_f32_e32 v8, v8, v72
	v_add_f32_e32 v9, v9, v73
	s_waitcnt lgkmcnt(0)
	v_fma_f32 v5, -2.0, v5, v2
	v_fma_f32 v6, -2.0, v6, v2
	v_fma_f32 v8, -2.0, v8, v2
	v_fmac_f32_e32 v2, -2.0, v9
	ds_write2st64_b32 v3, v5, v6 offset1:1
	ds_write2st64_b32 v3, v8, v2 offset0:2 offset1:3
	s_waitcnt lgkmcnt(0)
	s_barrier
	ds_read2_b32 v[2:3], v4 offset1:16
	ds_read2_b32 v[4:5], v4 offset0:32 offset1:48
	v_or_b32_e32 v6, 16, v138
	v_or_b32_e32 v8, 32, v138
	v_or_b32_e32 v9, 48, v138
	s_waitcnt lgkmcnt(1)
	v_cmp_lt_f32_e32 vcc, v3, v2
	s_nop 1
	v_cndmask_b32_e32 v10, v2, v3, vcc
	v_cndmask_b32_e32 v6, v138, v6, vcc
	s_waitcnt lgkmcnt(0)
	v_cmp_lt_f32_e32 vcc, v4, v10
	s_nop 1
	v_cndmask_b32_e32 v10, v10, v4, vcc
	v_cndmask_b32_e32 v8, v6, v8, vcc
	v_cmp_lt_f32_e32 vcc, v5, v10
	s_nop 1
	v_cndmask_b32_e32 v6, v10, v5, vcc
	v_cndmask_b32_e32 v14, v8, v9, vcc
	s_nop 0
	v_mov_b32_dpp v9, v6 quad_perm:[1,0,3,2] row_mask:0xf bank_mask:0xf bound_ctrl:1
	v_mov_b32_dpp v8, v14 quad_perm:[1,0,3,2] row_mask:0xf bank_mask:0xf bound_ctrl:1
	v_cmp_gt_f32_e64 s[4:5], v6, v9
	v_cmp_ngt_f32_e32 vcc, v6, v9
	s_and_saveexec_b64 s[6:7], vcc
	v_cmp_eq_f32_e32 vcc, v6, v9
	v_cmp_lt_i32_e64 s[0:1], v8, v14
	s_and_b64 s[0:1], vcc, s[0:1]
	s_andn2_b64 s[4:5], s[4:5], exec
	s_and_b64 s[0:1], s[0:1], exec
	s_or_b64 s[4:5], s[4:5], s[0:1]
	s_or_b64 exec, exec, s[6:7]
	s_and_saveexec_b64 s[0:1], s[4:5]
	v_mov_b32_e32 v6, v9
	v_mov_b32_e32 v14, v8
	s_or_b64 exec, exec, s[0:1]
	v_mov_b32_dpp v9, v6 quad_perm:[2,3,0,1] row_mask:0xf bank_mask:0xf bound_ctrl:1
	v_mov_b32_dpp v8, v14 quad_perm:[2,3,0,1] row_mask:0xf bank_mask:0xf bound_ctrl:1
	v_cmp_gt_f32_e64 s[4:5], v6, v9
	v_cmp_ngt_f32_e32 vcc, v6, v9
	s_and_saveexec_b64 s[6:7], vcc
	v_cmp_eq_f32_e32 vcc, v6, v9
	v_cmp_lt_i32_e64 s[0:1], v8, v14
	s_and_b64 s[0:1], vcc, s[0:1]
	s_andn2_b64 s[4:5], s[4:5], exec
	s_and_b64 s[0:1], s[0:1], exec
	s_or_b64 s[4:5], s[4:5], s[0:1]
	s_or_b64 exec, exec, s[6:7]
	s_and_saveexec_b64 s[0:1], s[4:5]
	v_mov_b32_e32 v6, v9
	v_mov_b32_e32 v14, v8
	s_or_b64 exec, exec, s[0:1]
	v_mov_b32_dpp v9, v6 row_half_mirror row_mask:0xf bank_mask:0xf bound_ctrl:1
	v_mov_b32_dpp v8, v14 row_half_mirror row_mask:0xf bank_mask:0xf bound_ctrl:1
	v_cmp_gt_f32_e64 s[4:5], v6, v9
	v_cmp_ngt_f32_e32 vcc, v6, v9
	s_and_saveexec_b64 s[6:7], vcc
	v_cmp_eq_f32_e32 vcc, v6, v9
	v_cmp_lt_i32_e64 s[0:1], v8, v14
	s_and_b64 s[0:1], vcc, s[0:1]
	s_andn2_b64 s[4:5], s[4:5], exec
	s_and_b64 s[0:1], s[0:1], exec
	s_or_b64 s[4:5], s[4:5], s[0:1]
	s_or_b64 exec, exec, s[6:7]
	s_and_saveexec_b64 s[0:1], s[4:5]
	v_mov_b32_e32 v6, v9
	v_mov_b32_e32 v14, v8
	s_or_b64 exec, exec, s[0:1]
	v_mov_b32_dpp v8, v6 row_mirror row_mask:0xf bank_mask:0xf bound_ctrl:1
	v_mov_b32_dpp v9, v14 row_mirror row_mask:0xf bank_mask:0xf bound_ctrl:1
	v_cmp_gt_f32_e64 s[4:5], v6, v8
	v_cmp_ngt_f32_e32 vcc, v6, v8
	s_and_saveexec_b64 s[6:7], vcc
	v_cmp_eq_f32_e32 vcc, v6, v8
	v_cmp_lt_i32_e64 s[0:1], v9, v14
	s_and_b64 s[0:1], vcc, s[0:1]
	s_andn2_b64 s[4:5], s[4:5], exec
	s_and_b64 s[0:1], s[0:1], exec
	s_or_b64 s[4:5], s[4:5], s[0:1]
	s_or_b64 exec, exec, s[6:7]
	s_and_saveexec_b64 s[0:1], s[4:5]
	v_mov_b32_e32 v6, v8
	v_mov_b32_e32 v14, v9
	s_or_b64 exec, exec, s[0:1]
	v_mov_b32_e32 v8, 0x11300
	v_lshl_or_b32 v8, v1, 2, v8
	ds_read_b32 v8, v8
	v_mov_b32_e32 v9, 0x11200
	v_lshl_add_u32 v7, v7, 2, v9
	ds_read_b32 v9, v7
	v_mov_b32_e32 v13, 0x260
	s_waitcnt lgkmcnt(1)
	v_mov_b32_dpp v7, v8 quad_perm:[1,0,3,2] row_mask:0xf bank_mask:0xf bound_ctrl:1
	v_max_f32_e32 v8, v8, v8
	v_max_f32_e32 v7, v7, v7
	v_max_f32_e32 v7, v8, v7
	v_lshlrev_b32_e32 v18, 2, v139
	v_mov_b32_e32 v19, 0
	v_mov_b32_dpp v8, v7 quad_perm:[2,3,0,1] row_mask:0xf bank_mask:0xf bound_ctrl:1
	v_max_f32_e32 v8, v8, v8
	v_max_f32_e32 v7, v7, v8
	s_mov_b32 s25, 0
	s_mov_b32 s26, s25
	v_mov_b32_dpp v8, v7 row_half_mirror row_mask:0xf bank_mask:0xf bound_ctrl:1
	v_max_f32_e32 v8, v8, v8
	v_max_f32_e32 v7, v7, v8
	s_nop 1
	v_mov_b32_dpp v8, v7 row_mirror row_mask:0xf bank_mask:0xf bound_ctrl:1
	v_max_f32_e32 v8, v8, v8
	v_max_f32_e32 v7, v7, v8
	s_nop 0
	v_readlane_b32 s4, v7, 32
	v_readlane_b32 s5, v7, 48
	v_readlane_b32 s0, v7, 0
	v_readlane_b32 s1, v7, 16
	v_max_f32_e64 v7, s5, s5
	v_max_f32_e64 v8, s4, s4
	v_max_f32_e32 v7, v8, v7
	v_mov_b32_e32 v8, s1
	v_max3_f32 v8, s0, v8, v7
	s_mov_b32 s0, 0x3f800347
	s_mov_b32 s1, 0x3f8020c5
	s_waitcnt lgkmcnt(0)
	v_pk_mul_f32 v[8:9], v[8:9], s[0:1]
	s_mov_b32 s4, 0xf800000
	v_mul_f32_e32 v7, 0x4f800000, v9
	v_cmp_gt_f32_e32 vcc, s4, v9
	s_nop 1
	v_cndmask_b32_e32 v7, v9, v7, vcc
	v_sqrt_f32_e32 v10, v7
	s_nop 0
	v_add_u32_e32 v11, -1, v10
	v_fma_f32 v12, -v11, v10, v7
	v_cmp_ge_f32_e64 s[0:1], 0, v12
	v_add_u32_e32 v12, 1, v10
	s_nop 0
	v_cndmask_b32_e64 v11, v10, v11, s[0:1]
	v_fma_f32 v10, -v12, v10, v7
	v_cmp_lt_f32_e64 s[0:1], 0, v10
	s_nop 1
	v_cndmask_b32_e64 v10, v11, v12, s[0:1]
	v_mul_f32_e32 v11, 0x37800000, v10
	v_cndmask_b32_e32 v10, v10, v11, vcc
	v_mul_f32_e32 v11, 0x4f800000, v8
	v_cmp_gt_f32_e32 vcc, s4, v8
	v_cmp_class_f32_e64 s[0:1], v7, v13
	s_nop 0
	v_cndmask_b32_e32 v11, v8, v11, vcc
	v_sqrt_f32_e32 v12, v11
	v_cndmask_b32_e64 v7, v10, v7, s[0:1]
	v_add_u32_e32 v10, -1, v12
	v_fma_f32 v15, -v10, v12, v11
	v_cmp_ge_f32_e64 s[0:1], 0, v15
	v_add_u32_e32 v15, 1, v12
	s_nop 0
	v_cndmask_b32_e64 v10, v12, v10, s[0:1]
	v_fma_f32 v12, -v15, v12, v11
	v_cmp_lt_f32_e64 s[0:1], 0, v12
	s_nop 1
	v_cndmask_b32_e64 v10, v10, v15, s[0:1]
	v_mul_f32_e32 v12, 0x37800000, v10
	v_cndmask_b32_e32 v10, v10, v12, vcc
	v_cmp_class_f32_e32 vcc, v11, v13
	s_mov_b32 s0, 0x380637bd
	s_mov_b32 s1, 0x350637bd
	v_cndmask_b32_e32 v10, v10, v11, vcc
	v_mul_f32_e32 v7, v7, v10
	v_mul_f32_e32 v7, 0x3f800347, v7
	v_pk_mul_f32 v[8:9], v[8:9], s[0:1]
	s_nop 0
	v_fmamk_f32 v7, v7, 0x3888509c, v9
	v_add_f32_e32 v7, v8, v7
	v_add_f32_e32 v7, 0xda24260, v7
	v_add_f32_e32 v6, v6, v7
	v_cmp_le_f32_e64 s[8:9], v2, v6
	v_cmp_le_f32_e64 s[6:7], v3, v6
	v_cmp_le_f32_e64 s[4:5], v4, v6
	v_lshl_add_u64 v[2:3], s[22:23], 0, v[18:19]
	s_and_b32 s19, s8, 0xffff
	s_lshl_b32 s22, s6, 16
	v_cmp_le_f32_e64 s[0:1], v5, v6
	s_or_b32 s24, s19, s22
	s_and_b32 s23, s4, 0xffff
	s_mov_b32 s22, s25
	s_or_b64 s[22:23], s[24:25], s[22:23]
	s_lshl_b32 s27, s0, 16
	s_or_b64 s[26:27], s[22:23], s[26:27]
	s_add_u32 s22, s26, -1
	s_addc_u32 s23, s27, -1
	s_and_b64 s[22:23], s[26:27], s[22:23]
	s_cmp_eq_u64 s[22:23], 0
	v_readlane_b32 s22, v14, 0
	s_cbranch_scc1 .LBB0_139
	s_lshl_b32 s19, s29, 2
	s_add_i32 s19, s19, 0x11100
	v_mov_b32_e32 v4, s19
	ds_read_b32 v4, v4
	s_mul_i32 s19, s17, 0x2040
	v_add_u32_e32 v8, s19, v135
	v_mov_b32_e32 v15, 0x7f800000
	s_waitcnt lgkmcnt(0)
	v_max_i32_e32 v4, 1, v4
	v_cvt_f64_u32_e32 v[12:13], v4
	v_div_scale_f64 v[16:17], s[30:31], v[12:13], v[12:13], 1.0
	v_rcp_f64_e32 v[20:21], v[16:17]
	v_div_scale_f64 v[22:23], vcc, 1.0, v[12:13], 1.0
	ds_read2st64_b64 v[4:7], v8 offset0:64 offset1:65
	ds_read2st64_b64 v[8:11], v8 offset0:66 offset1:67
	v_fma_f64 v[24:25], -v[16:17], v[20:21], 1.0
	v_fmac_f64_e32 v[20:21], v[20:21], v[24:25]
	v_fma_f64 v[24:25], -v[16:17], v[20:21], 1.0
	v_fmac_f64_e32 v[20:21], v[20:21], v[24:25]
	v_mul_f64 v[24:25], v[22:23], v[20:21]
	v_fma_f64 v[16:17], -v[16:17], v[24:25], v[22:23]
	v_div_fmas_f64 v[16:17], v[16:17], v[20:21], v[24:25]
	v_div_fixup_f64 v[12:13], v[16:17], v[12:13], 1.0
	s_waitcnt lgkmcnt(1)
	v_mul_f64 v[6:7], v[6:7], v[12:13]
	v_mul_f64 v[4:5], v[4:5], v[12:13]
	s_waitcnt lgkmcnt(0)
	v_mul_f64 v[8:9], v[8:9], v[12:13]
	v_mul_f64 v[10:11], v[12:13], v[10:11]
	v_mul_f64 v[12:13], v[6:7], v[6:7]
	v_fmac_f64_e32 v[12:13], v[4:5], v[4:5]
	v_fmac_f64_e32 v[12:13], v[8:9], v[8:9]
	v_fmac_f64_e32 v[12:13], v[10:11], v[10:11]
	s_nop 1
	v_mov_b32_dpp v16, v12 quad_perm:[1,0,3,2] row_mask:0xf bank_mask:0xf bound_ctrl:1
	v_mov_b32_dpp v17, v13 quad_perm:[1,0,3,2] row_mask:0xf bank_mask:0xf bound_ctrl:1
	v_add_f64 v[12:13], v[12:13], v[16:17]
	s_nop 1
	v_mov_b32_dpp v16, v12 quad_perm:[2,3,0,1] row_mask:0xf bank_mask:0xf bound_ctrl:1
	v_mov_b32_dpp v17, v13 quad_perm:[2,3,0,1] row_mask:0xf bank_mask:0xf bound_ctrl:1
	v_add_f64 v[12:13], v[12:13], v[16:17]
	s_nop 1
	v_mov_b32_dpp v16, v12 row_half_mirror row_mask:0xf bank_mask:0xf bound_ctrl:1
	v_mov_b32_dpp v17, v13 row_half_mirror row_mask:0xf bank_mask:0xf bound_ctrl:1
	v_add_f64 v[12:13], v[12:13], v[16:17]
	s_nop 1
	v_mov_b32_dpp v16, v12 row_mirror row_mask:0xf bank_mask:0xf bound_ctrl:1
	v_mov_b32_dpp v17, v13 row_mirror row_mask:0xf bank_mask:0xf bound_ctrl:1
	v_add_f64 v[12:13], v[12:13], v[16:17]
	s_nop 0
	v_readlane_b32 s19, v13, 16
	v_readlane_b32 s23, v12, 16
	v_readlane_b32 s31, v13, 0
	v_readlane_b32 s30, v12, 0
	v_mov_b32_e32 v16, s23
	v_mov_b32_e32 v17, s19
	v_readlane_b32 s19, v13, 48
	v_readlane_b32 s23, v12, 48
	v_add_f64 v[16:17], s[30:31], v[16:17]
	v_readlane_b32 s31, v13, 32
	v_readlane_b32 s30, v12, 32
	v_mov_b32_e32 v12, s23
	v_mov_b32_e32 v13, s19
	v_add_f64 v[12:13], s[30:31], v[12:13]
	v_add_f64 v[12:13], v[16:17], v[12:13]

	.amdhsa_kernel _Z7vq_mainPKfPKiS0_PfPhPdPi
		.amdhsa_group_segment_fixed_size 71936
		.amdhsa_private_segment_fixed_size 0
		.amdhsa_kernarg_size 56
		.amdhsa_user_sgpr_count 2
		.amdhsa_user_sgpr_dispatch_ptr 0
		.amdhsa_user_sgpr_queue_ptr 0
		.amdhsa_user_sgpr_kernarg_segment_ptr 1
		.amdhsa_user_sgpr_dispatch_id 0
		.amdhsa_user_sgpr_kernarg_preload_length 0
		.amdhsa_user_sgpr_kernarg_preload_offset 0
		.amdhsa_user_sgpr_private_segment_size 0
		.amdhsa_uses_dynamic_stack 0
		.amdhsa_enable_private_segment 0
		.amdhsa_system_sgpr_workgroup_id_x 1
		.amdhsa_system_sgpr_workgroup_id_y 0
		.amdhsa_system_sgpr_workgroup_id_z 0
		.amdhsa_system_sgpr_workgroup_info 0
		.amdhsa_system_vgpr_workitem_id 0
		.amdhsa_next_free_vgpr 232
		.amdhsa_next_free_sgpr 102
		.amdhsa_accum_offset 224
		.amdhsa_reserve_vcc 1
		.amdhsa_float_round_mode_32 0
		.amdhsa_float_round_mode_16_64 0
		.amdhsa_float_denorm_mode_32 3
		.amdhsa_float_denorm_mode_16_64 3
		.amdhsa_dx10_clamp 1
		.amdhsa_ieee_mode 1
		.amdhsa_fp16_overflow 0
		.amdhsa_tg_split 0
		.amdhsa_exception_fp_ieee_invalid_op 0
		.amdhsa_exception_fp_denorm_src 0
		.amdhsa_exception_fp_ieee_div_zero 0
		.amdhsa_exception_fp_ieee_overflow 0
		.amdhsa_exception_fp_ieee_underflow 0
		.amdhsa_exception_fp_ieee_inexact 0
		.amdhsa_exception_int_div_zero 0
	.end_amdhsa_kernel

amdhsa.kernels:
  - .agpr_count:     8
    .args:
      - .actual_access:  read_only
        .address_space:  global
        .offset:         0
        .size:           8
        .value_kind:     global_buffer
      - .actual_access:  read_only
        .address_space:  global
        .offset:         8
        .size:           8
        .value_kind:     global_buffer
      - .actual_access:  read_only
        .address_space:  global
        .offset:         16
        .size:           8
        .value_kind:     global_buffer
      - .actual_access:  write_only
        .address_space:  global
        .offset:         24
        .size:           8
        .value_kind:     global_buffer
      - .actual_access:  write_only
        .address_space:  global
        .offset:         32
        .size:           8
        .value_kind:     global_buffer
      - .actual_access:  write_only
        .address_space:  global
        .offset:         40
        .size:           8
        .value_kind:     global_buffer
      - .actual_access:  write_only
        .address_space:  global
        .offset:         48
        .size:           8
        .value_kind:     global_buffer
    .group_segment_fixed_size: 71936
    .kernarg_segment_align: 8
    .kernarg_segment_size: 56
    .language:       OpenCL C
    .language_version:
      - 2
      - 0
    .max_flat_workgroup_size: 256
    .name:           _Z7vq_mainPKfPKiS0_PfPhPdPi
    .private_segment_fixed_size: 0
    .sgpr_count:     108
    .sgpr_spill_count: 0
    .symbol:         _Z7vq_mainPKfPKiS0_PfPhPdPi.kd
    .uniform_work_group_size: 1
    .uses_dynamic_stack: false
    .vgpr_count:     232
    .vgpr_spill_count: 0
    .wavefront_size: 64
  - .agpr_count:     0
    .args:
      - .actual_access:  read_only
        .address_space:  global
        .offset:         0
        .size:           8
        .value_kind:     global_buffer
      - .actual_access:  read_only
        .address_space:  global
        .offset:         8
        .size:           8
        .value_kind:     global_buffer
      - .actual_access:  read_only
        .address_space:  global
        .offset:         16
        .size:           8
        .value_kind:     global_buffer
      - .actual_access:  write_only
        .address_space:  global
        .offset:         24
        .size:           8
        .value_kind:     global_buffer
    .group_segment_fixed_size: 352
    .kernarg_segment_align: 8
    .kernarg_segment_size: 32
    .language:       OpenCL C
    .language_version:
      - 2
      - 0
    .max_flat_workgroup_size: 1024
    .name:           _Z11vq_finalizePK15HIP_vector_typeIjLj4EEPKdPKiPf
    .private_segment_fixed_size: 0
    .sgpr_count:     30
    .sgpr_spill_count: 0
    .symbol:         _Z11vq_finalizePK15HIP_vector_typeIjLj4EEPKdPKiPf.kd
    .uniform_work_group_size: 1
    .uses_dynamic_stack: false
    .vgpr_count:     24
    .vgpr_spill_count: 0
    .wavefront_size: 64
